# baseline (speedup 1.0000x reference)
_ZN12_GLOBAL__N_110qkv_kernelEPKfPKDF16_S1_S1_S1_PKiS5_S1_PDF16_S6_S6_:
	v_mov_b32_e32 v251, v0
	s_bfe_u32 s60, s2, 0x30003
	s_load_dwordx2 s[26:27], s[0:1], 0x50
	s_load_dwordx4 s[40:43], s[0:1], 0x0
	s_cmpk_lt_u32 s2, 0x70
	s_cbranch_scc1 .Lmy_kvjob
	s_cmpk_lt_u32 s2, 0xf0
	s_cbranch_scc1 .Lmy_qjob
	s_cmpk_lt_u32 s2, 0x160
	s_cbranch_scc1 .Lmy_kvjob2
	s_endpgm
.Lmy_kvjob2:
	s_add_i32 s2, s2, 0xffffff80
	s_branch .Lmy_kvjob
.Lmy_qjob:
	s_add_i32 s2, s2, 0xffffff90
	s_and_b32 s4, s2, 7
	s_lshr_b32 s5, s2, 3
	s_and_b32 s6, s5, 1
	s_lshl_b32 s34, s6, 8
	s_lshr_b32 s5, s5, 1
	s_lshl_b32 s5, s5, 3
	s_or_b32 s5, s5, s4
	s_lshl_b32 s33, s5, 7
	s_lshr_b32 s28, s33, 11
	s_mov_b32 s36, 0
	s_waitcnt lgkmcnt(0)
	v_lshrrev_b32_e32 v247, 3, v251
	v_and_b32_e32 v248, 7, v251
	v_lshlrev_b32_e32 v248, 4, v248
	v_lshl_add_u32 v218, v247, 10, v248
	s_lshl_b32 s7, s34, 10
	s_add_u32 s44, s42, s7
	s_addc_u32 s45, s43, 0
	s_add_u32 s46, s44, 0x10000
	s_addc_u32 s47, s45, 0
	s_add_u32 s48, s44, 0x20000
	s_addc_u32 s49, s45, 0
	s_add_u32 s58, s44, 0x30000
	s_addc_u32 s59, s45, 0
	global_load_dwordx4 v[144:147], v218, s[44:45] offset:0
	global_load_dwordx4 v[148:151], v218, s[46:47] offset:0
	global_load_dwordx4 v[152:155], v218, s[48:49] offset:0
	global_load_dwordx4 v[156:159], v218, s[58:59] offset:0
	global_load_dwordx4 v[180:183], v218, s[44:45] offset:128
	global_load_dwordx4 v[184:187], v218, s[46:47] offset:128
	global_load_dwordx4 v[188:191], v218, s[48:49] offset:128
	global_load_dwordx4 v[192:195], v218, s[58:59] offset:128
	v_lshrrev_b32_e32 v240, 4, v251
	v_add_u32_e32 v240, s33, v240
	v_and_b32_e32 v241, 15, v251
	v_lshlrev_b32_e32 v241, 4, v241
	v_lshl_add_u32 v219, v240, 11, v241
	v_add_u32_e32 v220, 0x10000, v219
	v_add_u32_e32 v221, 0x20000, v219
	v_add_u32_e32 v222, 0x30000, v219
	v_mov_b32_e32 v223, v219
	s_branch .Lmy_common
